# readout: bilinear re-associated, P = e@Wb computed early with v_readlane broadcast; phase1 stores Wb copy
# baseline (speedup 1.0000x reference)
_Z8k_phase1PKfS0_S0_PDv4_jS2_PiS3_P15HIP_vector_typeIiLj2EES0_Pf:
	s_cmp_gt_i32 s2, 7
	s_mov_b64 s[4:5], -1
	s_cbranch_scc0 .LBB0_26
	s_cmpk_gt_u32 s2, 0x187
	s_cbranch_scc0 .LBB0_7
	s_lshl_b32 s3, s2, 8
	s_cmpk_gt_u32 s2, 0x18f
	v_add_u32_e32 v1, s3, v0
	s_cbranch_scc0 .LBB0_4
	s_load_dwordx4 s[4:7], s[0:1], 0x40
	v_add_u32_e32 v2, 0xfffe7000, v1
	v_lshlrev_b32_e32 v3, 2, v2
	s_waitcnt lgkmcnt(0)
	global_load_dword v4, v3, s[4:5]
	v_mov_b32_e32 v3, 0
	v_lshl_add_u64 v[2:3], v[2:3], 2, s[6:7]
	s_mov_b64 s[4:5], 0
	s_waitcnt vmcnt(0)
	global_store_dword v[2:3], v4, off

_Z9k_readoutPKDv4_jPKfPKiPK15HIP_vector_typeIiLj2EES3_S3_S3_PfSA_:
	s_load_dwordx4 s[4:7], s[0:1], 0x0
	s_load_dwordx2 s[8:9], s[0:1], 0x10
	v_lshrrev_b32_e32 v53, 6, v0
	v_lshl_or_b32 v44, s2, 2, v53
	v_ashrrev_i32_e32 v45, 31, v44
	v_and_b32_e32 v52, 63, v0
	s_waitcnt lgkmcnt(0)
	v_lshl_add_u64 v[2:3], v[44:45], 2, s[8:9]
	global_load_dword v57, v[2:3], off
	v_mov_b32_e32 v9, 0
	v_lshlrev_b64 v[2:3], 8, v[44:45]
	v_lshl_add_u64 v[2:3], s[6:7], 0, v[2:3]
	v_lshlrev_b32_e32 v46, 2, v52
	v_mov_b32_e32 v47, v9
	v_lshl_add_u64 v[2:3], v[2:3], 0, v[46:47]
	v_add_co_u32_e32 v4, vcc, 0x200000, v2
	s_load_dwordx2 s[6:7], s[0:1], 0x30
	s_nop 0
	v_addc_co_u32_e32 v5, vcc, 0, v3, vcc
	global_load_dword v48, v[2:3], off
	global_load_dword v49, v[4:5], off
	v_bfe_u32 v54, v0, 5, 1
	s_waitcnt lgkmcnt(0)
	s_load_dword s2, s[6:7], 0x0
	s_movk_i32 s6, 0x80
	v_and_b32_e32 v47, 7, v0
	v_lshlrev_b32_e32 v8, 20, v54
	s_mov_b32 s3, 0
	v_bfe_u32 v55, v0, 3, 2
	v_mbcnt_lo_u32_b32 v56, -1, 0
	s_waitcnt vmcnt(2)
	v_cmp_lt_i32_e32 vcc, s6, v57
	s_and_saveexec_b64 s[6:7], vcc
	s_xor_b64 s[6:7], exec, s[6:7]
	s_cbranch_execz .LBB4_10
	s_load_dwordx2 s[28:29], s[0:1], 0x28
	v_mov_b32_e32 v92, 0
	v_mov_b32_e32 v93, 0
	s_waitcnt lgkmcnt(0)
	global_load_dword v60, v46, s[28:29]
	global_load_dword v61, v46, s[28:29] offset:256
	global_load_dword v62, v46, s[28:29] offset:512
	global_load_dword v63, v46, s[28:29] offset:768
	global_load_dword v64, v46, s[28:29] offset:1024
	global_load_dword v65, v46, s[28:29] offset:1280
	global_load_dword v66, v46, s[28:29] offset:1536
	global_load_dword v67, v46, s[28:29] offset:1792
	global_load_dword v68, v46, s[28:29] offset:2048
	global_load_dword v69, v46, s[28:29] offset:2304
	global_load_dword v70, v46, s[28:29] offset:2560
	global_load_dword v71, v46, s[28:29] offset:2816
	global_load_dword v72, v46, s[28:29] offset:3072
	global_load_dword v73, v46, s[28:29] offset:3328
	global_load_dword v74, v46, s[28:29] offset:3584
	global_load_dword v75, v46, s[28:29] offset:3840
	s_add_u32 s28, s28, 0x1000
	s_addc_u32 s29, s29, 0
	global_load_dword v76, v46, s[28:29]
	global_load_dword v77, v46, s[28:29] offset:256
	global_load_dword v78, v46, s[28:29] offset:512
	global_load_dword v79, v46, s[28:29] offset:768
	global_load_dword v80, v46, s[28:29] offset:1024
	global_load_dword v81, v46, s[28:29] offset:1280
	global_load_dword v82, v46, s[28:29] offset:1536
	global_load_dword v83, v46, s[28:29] offset:1792
	global_load_dword v84, v46, s[28:29] offset:2048
	global_load_dword v85, v46, s[28:29] offset:2304
	global_load_dword v86, v46, s[28:29] offset:2560
	global_load_dword v87, v46, s[28:29] offset:2816
	global_load_dword v88, v46, s[28:29] offset:3072
	global_load_dword v89, v46, s[28:29] offset:3328
	global_load_dword v90, v46, s[28:29] offset:3584
	global_load_dword v91, v46, s[28:29] offset:3840
	s_add_u32 s28, s28, 0x1000
	s_addc_u32 s29, s29, 0
	s_waitcnt vmcnt(31)
	v_readlane_b32 s12, v48, 0
	v_readlane_b32 s13, v49, 0
	v_readlane_b32 s14, v48, 1
	v_readlane_b32 s15, v49, 1
	v_readlane_b32 s16, v48, 2
	v_readlane_b32 s17, v49, 2
	v_readlane_b32 s18, v48, 3
	v_readlane_b32 s19, v49, 3
	v_readlane_b32 s20, v48, 4
	v_readlane_b32 s21, v49, 4
	v_readlane_b32 s22, v48, 5
	v_readlane_b32 s23, v49, 5
	v_readlane_b32 s24, v48, 6
	v_readlane_b32 s25, v49, 6
	v_readlane_b32 s26, v48, 7
	v_readlane_b32 s27, v49, 7
	s_waitcnt vmcnt(31)
	v_fmac_f32_e32 v92, s12, v60
	v_fmac_f32_e32 v93, s13, v60
	s_waitcnt vmcnt(30)
	v_fmac_f32_e32 v92, s14, v61
	v_fmac_f32_e32 v93, s15, v61
	s_waitcnt vmcnt(29)
	v_fmac_f32_e32 v92, s16, v62
	v_fmac_f32_e32 v93, s17, v62
	s_waitcnt vmcnt(28)
	v_fmac_f32_e32 v92, s18, v63
	v_fmac_f32_e32 v93, s19, v63
	s_waitcnt vmcnt(27)
	v_fmac_f32_e32 v92, s20, v64
	v_fmac_f32_e32 v93, s21, v64
	s_waitcnt vmcnt(26)
	v_fmac_f32_e32 v92, s22, v65
	v_fmac_f32_e32 v93, s23, v65
	s_waitcnt vmcnt(25)
	v_fmac_f32_e32 v92, s24, v66
	v_fmac_f32_e32 v93, s25, v66
	s_waitcnt vmcnt(24)
	v_fmac_f32_e32 v92, s26, v67
	v_fmac_f32_e32 v93, s27, v67
	v_readlane_b32 s12, v48, 8
	v_readlane_b32 s13, v49, 8
	v_readlane_b32 s14, v48, 9
	v_readlane_b32 s15, v49, 9
	v_readlane_b32 s16, v48, 10
	v_readlane_b32 s17, v49, 10
	v_readlane_b32 s18, v48, 11
	v_readlane_b32 s19, v49, 11
	v_readlane_b32 s20, v48, 12
	v_readlane_b32 s21, v49, 12
	v_readlane_b32 s22, v48, 13
	v_readlane_b32 s23, v49, 13
	v_readlane_b32 s24, v48, 14
	v_readlane_b32 s25, v49, 14
	v_readlane_b32 s26, v48, 15
	v_readlane_b32 s27, v49, 15
	s_waitcnt vmcnt(23)
	v_fmac_f32_e32 v92, s12, v68
	v_fmac_f32_e32 v93, s13, v68
	s_waitcnt vmcnt(22)
	v_fmac_f32_e32 v92, s14, v69
	v_fmac_f32_e32 v93, s15, v69
	s_waitcnt vmcnt(21)
	v_fmac_f32_e32 v92, s16, v70
	v_fmac_f32_e32 v93, s17, v70
	s_waitcnt vmcnt(20)
	v_fmac_f32_e32 v92, s18, v71
	v_fmac_f32_e32 v93, s19, v71
	s_waitcnt vmcnt(19)
	v_fmac_f32_e32 v92, s20, v72
	v_fmac_f32_e32 v93, s21, v72
	s_waitcnt vmcnt(18)
	v_fmac_f32_e32 v92, s22, v73
	v_fmac_f32_e32 v93, s23, v73
	s_waitcnt vmcnt(17)
	v_fmac_f32_e32 v92, s24, v74
	v_fmac_f32_e32 v93, s25, v74
	s_waitcnt vmcnt(16)
	v_fmac_f32_e32 v92, s26, v75
	v_fmac_f32_e32 v93, s27, v75
	global_load_dword v60, v46, s[28:29]
	global_load_dword v61, v46, s[28:29] offset:256
	global_load_dword v62, v46, s[28:29] offset:512
	global_load_dword v63, v46, s[28:29] offset:768
	global_load_dword v64, v46, s[28:29] offset:1024
	global_load_dword v65, v46, s[28:29] offset:1280
	global_load_dword v66, v46, s[28:29] offset:1536
	global_load_dword v67, v46, s[28:29] offset:1792
	global_load_dword v68, v46, s[28:29] offset:2048
	global_load_dword v69, v46, s[28:29] offset:2304
	global_load_dword v70, v46, s[28:29] offset:2560
	global_load_dword v71, v46, s[28:29] offset:2816
	global_load_dword v72, v46, s[28:29] offset:3072
	global_load_dword v73, v46, s[28:29] offset:3328
	global_load_dword v74, v46, s[28:29] offset:3584
	global_load_dword v75, v46, s[28:29] offset:3840
	s_add_u32 s28, s28, 0x1000
	s_addc_u32 s29, s29, 0
	v_readlane_b32 s12, v48, 16
	v_readlane_b32 s13, v49, 16
	v_readlane_b32 s14, v48, 17
	v_readlane_b32 s15, v49, 17
	v_readlane_b32 s16, v48, 18
	v_readlane_b32 s17, v49, 18
	v_readlane_b32 s18, v48, 19
	v_readlane_b32 s19, v49, 19
	v_readlane_b32 s20, v48, 20
	v_readlane_b32 s21, v49, 20
	v_readlane_b32 s22, v48, 21
	v_readlane_b32 s23, v49, 21
	v_readlane_b32 s24, v48, 22
	v_readlane_b32 s25, v49, 22
	v_readlane_b32 s26, v48, 23
	v_readlane_b32 s27, v49, 23
	s_waitcnt vmcnt(31)
	v_fmac_f32_e32 v92, s12, v76
	v_fmac_f32_e32 v93, s13, v76
	s_waitcnt vmcnt(30)
	v_fmac_f32_e32 v92, s14, v77
	v_fmac_f32_e32 v93, s15, v77
	s_waitcnt vmcnt(29)
	v_fmac_f32_e32 v92, s16, v78
	v_fmac_f32_e32 v93, s17, v78
	s_waitcnt vmcnt(28)
	v_fmac_f32_e32 v92, s18, v79
	v_fmac_f32_e32 v93, s19, v79
	s_waitcnt vmcnt(27)
	v_fmac_f32_e32 v92, s20, v80
	v_fmac_f32_e32 v93, s21, v80
	s_waitcnt vmcnt(26)
	v_fmac_f32_e32 v92, s22, v81
	v_fmac_f32_e32 v93, s23, v81
	s_waitcnt vmcnt(25)
	v_fmac_f32_e32 v92, s24, v82
	v_fmac_f32_e32 v93, s25, v82
	s_waitcnt vmcnt(24)
	v_fmac_f32_e32 v92, s26, v83
	v_fmac_f32_e32 v93, s27, v83
	v_readlane_b32 s12, v48, 24
	v_readlane_b32 s13, v49, 24
	v_readlane_b32 s14, v48, 25
	v_readlane_b32 s15, v49, 25
	v_readlane_b32 s16, v48, 26
	v_readlane_b32 s17, v49, 26
	v_readlane_b32 s18, v48, 27
	v_readlane_b32 s19, v49, 27
	v_readlane_b32 s20, v48, 28
	v_readlane_b32 s21, v49, 28
	v_readlane_b32 s22, v48, 29
	v_readlane_b32 s23, v49, 29
	v_readlane_b32 s24, v48, 30
	v_readlane_b32 s25, v49, 30
	v_readlane_b32 s26, v48, 31
	v_readlane_b32 s27, v49, 31
	s_waitcnt vmcnt(23)
	v_fmac_f32_e32 v92, s12, v84
	v_fmac_f32_e32 v93, s13, v84
	s_waitcnt vmcnt(22)
	v_fmac_f32_e32 v92, s14, v85
	v_fmac_f32_e32 v93, s15, v85
	s_waitcnt vmcnt(21)
	v_fmac_f32_e32 v92, s16, v86
	v_fmac_f32_e32 v93, s17, v86
	s_waitcnt vmcnt(20)
	v_fmac_f32_e32 v92, s18, v87
	v_fmac_f32_e32 v93, s19, v87
	s_waitcnt vmcnt(19)
	v_fmac_f32_e32 v92, s20, v88
	v_fmac_f32_e32 v93, s21, v88
	s_waitcnt vmcnt(18)
	v_fmac_f32_e32 v92, s22, v89
	v_fmac_f32_e32 v93, s23, v89
	s_waitcnt vmcnt(17)
	v_fmac_f32_e32 v92, s24, v90
	v_fmac_f32_e32 v93, s25, v90
	s_waitcnt vmcnt(16)
	v_fmac_f32_e32 v92, s26, v91
	v_fmac_f32_e32 v93, s27, v91
	global_load_dword v76, v46, s[28:29]
	global_load_dword v77, v46, s[28:29] offset:256
	global_load_dword v78, v46, s[28:29] offset:512
	global_load_dword v79, v46, s[28:29] offset:768
	global_load_dword v80, v46, s[28:29] offset:1024
	global_load_dword v81, v46, s[28:29] offset:1280
	global_load_dword v82, v46, s[28:29] offset:1536
	global_load_dword v83, v46, s[28:29] offset:1792
	global_load_dword v84, v46, s[28:29] offset:2048
	global_load_dword v85, v46, s[28:29] offset:2304
	global_load_dword v86, v46, s[28:29] offset:2560
	global_load_dword v87, v46, s[28:29] offset:2816
	global_load_dword v88, v46, s[28:29] offset:3072
	global_load_dword v89, v46, s[28:29] offset:3328
	global_load_dword v90, v46, s[28:29] offset:3584
	global_load_dword v91, v46, s[28:29] offset:3840
	v_readlane_b32 s12, v48, 32
	v_readlane_b32 s13, v49, 32
	v_readlane_b32 s14, v48, 33
	v_readlane_b32 s15, v49, 33
	v_readlane_b32 s16, v48, 34
	v_readlane_b32 s17, v49, 34
	v_readlane_b32 s18, v48, 35
	v_readlane_b32 s19, v49, 35
	v_readlane_b32 s20, v48, 36
	v_readlane_b32 s21, v49, 36
	v_readlane_b32 s22, v48, 37
	v_readlane_b32 s23, v49, 37
	v_readlane_b32 s24, v48, 38
	v_readlane_b32 s25, v49, 38
	v_readlane_b32 s26, v48, 39
	v_readlane_b32 s27, v49, 39
	s_waitcnt vmcnt(31)
	v_fmac_f32_e32 v92, s12, v60
	v_fmac_f32_e32 v93, s13, v60
	s_waitcnt vmcnt(30)
	v_fmac_f32_e32 v92, s14, v61
	v_fmac_f32_e32 v93, s15, v61
	s_waitcnt vmcnt(29)
	v_fmac_f32_e32 v92, s16, v62
	v_fmac_f32_e32 v93, s17, v62
	s_waitcnt vmcnt(28)
	v_fmac_f32_e32 v92, s18, v63
	v_fmac_f32_e32 v93, s19, v63
	s_waitcnt vmcnt(27)
	v_fmac_f32_e32 v92, s20, v64
	v_fmac_f32_e32 v93, s21, v64
	s_waitcnt vmcnt(26)
	v_fmac_f32_e32 v92, s22, v65
	v_fmac_f32_e32 v93, s23, v65
	s_waitcnt vmcnt(25)
	v_fmac_f32_e32 v92, s24, v66
	v_fmac_f32_e32 v93, s25, v66
	s_waitcnt vmcnt(24)
	v_fmac_f32_e32 v92, s26, v67
	v_fmac_f32_e32 v93, s27, v67
	v_readlane_b32 s12, v48, 40
	v_readlane_b32 s13, v49, 40
	v_readlane_b32 s14, v48, 41
	v_readlane_b32 s15, v49, 41
	v_readlane_b32 s16, v48, 42
	v_readlane_b32 s17, v49, 42
	v_readlane_b32 s18, v48, 43
	v_readlane_b32 s19, v49, 43
	v_readlane_b32 s20, v48, 44
	v_readlane_b32 s21, v49, 44
	v_readlane_b32 s22, v48, 45
	v_readlane_b32 s23, v49, 45
	v_readlane_b32 s24, v48, 46
	v_readlane_b32 s25, v49, 46
	v_readlane_b32 s26, v48, 47
	v_readlane_b32 s27, v49, 47
	s_waitcnt vmcnt(23)
	v_fmac_f32_e32 v92, s12, v68
	v_fmac_f32_e32 v93, s13, v68
	s_waitcnt vmcnt(22)
	v_fmac_f32_e32 v92, s14, v69
	v_fmac_f32_e32 v93, s15, v69
	s_waitcnt vmcnt(21)
	v_fmac_f32_e32 v92, s16, v70
	v_fmac_f32_e32 v93, s17, v70
	s_waitcnt vmcnt(20)
	v_fmac_f32_e32 v92, s18, v71
	v_fmac_f32_e32 v93, s19, v71
	s_waitcnt vmcnt(19)
	v_fmac_f32_e32 v92, s20, v72
	v_fmac_f32_e32 v93, s21, v72
	s_waitcnt vmcnt(18)
	v_fmac_f32_e32 v92, s22, v73
	v_fmac_f32_e32 v93, s23, v73
	s_waitcnt vmcnt(17)
	v_fmac_f32_e32 v92, s24, v74
	v_fmac_f32_e32 v93, s25, v74
	s_waitcnt vmcnt(16)
	v_fmac_f32_e32 v92, s26, v75
	v_fmac_f32_e32 v93, s27, v75
	v_readlane_b32 s12, v48, 48
	v_readlane_b32 s13, v49, 48
	v_readlane_b32 s14, v48, 49
	v_readlane_b32 s15, v49, 49
	v_readlane_b32 s16, v48, 50
	v_readlane_b32 s17, v49, 50
	v_readlane_b32 s18, v48, 51
	v_readlane_b32 s19, v49, 51
	v_readlane_b32 s20, v48, 52
	v_readlane_b32 s21, v49, 52
	v_readlane_b32 s22, v48, 53
	v_readlane_b32 s23, v49, 53
	v_readlane_b32 s24, v48, 54
	v_readlane_b32 s25, v49, 54
	v_readlane_b32 s26, v48, 55
	v_readlane_b32 s27, v49, 55
	s_waitcnt vmcnt(15)
	v_fmac_f32_e32 v92, s12, v76
	v_fmac_f32_e32 v93, s13, v76
	s_waitcnt vmcnt(14)
	v_fmac_f32_e32 v92, s14, v77
	v_fmac_f32_e32 v93, s15, v77
	s_waitcnt vmcnt(13)
	v_fmac_f32_e32 v92, s16, v78
	v_fmac_f32_e32 v93, s17, v78
	s_waitcnt vmcnt(12)
	v_fmac_f32_e32 v92, s18, v79
	v_fmac_f32_e32 v93, s19, v79
	s_waitcnt vmcnt(11)
	v_fmac_f32_e32 v92, s20, v80
	v_fmac_f32_e32 v93, s21, v80
	s_waitcnt vmcnt(10)
	v_fmac_f32_e32 v92, s22, v81
	v_fmac_f32_e32 v93, s23, v81
	s_waitcnt vmcnt(9)
	v_fmac_f32_e32 v92, s24, v82
	v_fmac_f32_e32 v93, s25, v82
	s_waitcnt vmcnt(8)
	v_fmac_f32_e32 v92, s26, v83
	v_fmac_f32_e32 v93, s27, v83
	v_readlane_b32 s12, v48, 56
	v_readlane_b32 s13, v49, 56
	v_readlane_b32 s14, v48, 57
	v_readlane_b32 s15, v49, 57
	v_readlane_b32 s16, v48, 58
	v_readlane_b32 s17, v49, 58
	v_readlane_b32 s18, v48, 59
	v_readlane_b32 s19, v49, 59
	v_readlane_b32 s20, v48, 60
	v_readlane_b32 s21, v49, 60
	v_readlane_b32 s22, v48, 61
	v_readlane_b32 s23, v49, 61
	v_readlane_b32 s24, v48, 62
	v_readlane_b32 s25, v49, 62
	v_readlane_b32 s26, v48, 63
	v_readlane_b32 s27, v49, 63
	s_waitcnt vmcnt(7)
	v_fmac_f32_e32 v92, s12, v84
	v_fmac_f32_e32 v93, s13, v84
	s_waitcnt vmcnt(6)
	v_fmac_f32_e32 v92, s14, v85
	v_fmac_f32_e32 v93, s15, v85
	s_waitcnt vmcnt(5)
	v_fmac_f32_e32 v92, s16, v86
	v_fmac_f32_e32 v93, s17, v86
	s_waitcnt vmcnt(4)
	v_fmac_f32_e32 v92, s18, v87
	v_fmac_f32_e32 v93, s19, v87
	s_waitcnt vmcnt(3)
	v_fmac_f32_e32 v92, s20, v88
	v_fmac_f32_e32 v93, s21, v88
	s_waitcnt vmcnt(2)
	v_fmac_f32_e32 v92, s22, v89
	v_fmac_f32_e32 v93, s23, v89
	s_waitcnt vmcnt(1)
	v_fmac_f32_e32 v92, s24, v90
	v_fmac_f32_e32 v93, s25, v90
	s_waitcnt vmcnt(0)
	v_fmac_f32_e32 v92, s26, v91
	v_fmac_f32_e32 v93, s27, v91
	s_load_dwordx2 s[8:9], s[0:1], 0x20
	v_lshl_add_u64 v[0:1], s[4:5], 0, v[8:9]
	v_lshlrev_b32_e32 v8, 4, v47
	v_lshlrev_b64 v[2:3], 15, v[44:45]
	v_lshl_add_u64 v[16:17], v[0:1], 0, v[8:9]
	v_mbcnt_hi_u32_b32 v1, -1, v56
	s_waitcnt lgkmcnt(0)
	v_lshl_add_u64 v[18:19], s[8:9], 0, v[2:3]
	v_lshlrev_b32_e32 v0, 2, v55
	v_mov_b32_e32 v8, v9
	v_lshlrev_b32_e32 v1, 2, v1
	s_movk_i32 s8, 0x100
	v_mov_b32_e32 v10, v9
	v_mov_b32_e32 v11, v9
	v_mov_b32_e32 v12, v9
	v_mov_b32_e32 v13, v9
	v_mov_b32_e32 v14, v9
	v_mov_b32_e32 v15, v9
	v_and_or_b32 v23, v1, s8, v0
	v_mov_b64_e32 v[0:1], v[8:9]
	v_mov_b32_e32 v22, 0
	v_mov_b64_e32 v[2:3], v[10:11]
	v_mov_b64_e32 v[4:5], v[12:13]
	v_mov_b64_e32 v[6:7], v[14:15]

.LBB4_13:
	s_or_b64 exec, exec, s[8:9]
	s_load_dwordx2 s[28:29], s[0:1], 0x28
	v_mov_b32_e32 v92, 0
	v_mov_b32_e32 v93, 0
	s_waitcnt lgkmcnt(0)
	global_load_dword v60, v46, s[28:29]
	global_load_dword v61, v46, s[28:29] offset:256
	global_load_dword v62, v46, s[28:29] offset:512
	global_load_dword v63, v46, s[28:29] offset:768
	global_load_dword v64, v46, s[28:29] offset:1024
	global_load_dword v65, v46, s[28:29] offset:1280
	global_load_dword v66, v46, s[28:29] offset:1536
	global_load_dword v67, v46, s[28:29] offset:1792
	global_load_dword v68, v46, s[28:29] offset:2048
	global_load_dword v69, v46, s[28:29] offset:2304
	global_load_dword v70, v46, s[28:29] offset:2560
	global_load_dword v71, v46, s[28:29] offset:2816
	global_load_dword v72, v46, s[28:29] offset:3072
	global_load_dword v73, v46, s[28:29] offset:3328
	global_load_dword v74, v46, s[28:29] offset:3584
	global_load_dword v75, v46, s[28:29] offset:3840
	s_add_u32 s28, s28, 0x1000
	s_addc_u32 s29, s29, 0
	global_load_dword v76, v46, s[28:29]
	global_load_dword v77, v46, s[28:29] offset:256
	global_load_dword v78, v46, s[28:29] offset:512
	global_load_dword v79, v46, s[28:29] offset:768
	global_load_dword v80, v46, s[28:29] offset:1024
	global_load_dword v81, v46, s[28:29] offset:1280
	global_load_dword v82, v46, s[28:29] offset:1536
	global_load_dword v83, v46, s[28:29] offset:1792
	global_load_dword v84, v46, s[28:29] offset:2048
	global_load_dword v85, v46, s[28:29] offset:2304
	global_load_dword v86, v46, s[28:29] offset:2560
	global_load_dword v87, v46, s[28:29] offset:2816
	global_load_dword v88, v46, s[28:29] offset:3072
	global_load_dword v89, v46, s[28:29] offset:3328
	global_load_dword v90, v46, s[28:29] offset:3584
	global_load_dword v91, v46, s[28:29] offset:3840
	s_add_u32 s28, s28, 0x1000
	s_addc_u32 s29, s29, 0
	s_waitcnt vmcnt(31)
	v_readlane_b32 s12, v48, 0
	v_readlane_b32 s13, v49, 0
	v_readlane_b32 s14, v48, 1
	v_readlane_b32 s15, v49, 1
	v_readlane_b32 s16, v48, 2
	v_readlane_b32 s17, v49, 2
	v_readlane_b32 s18, v48, 3
	v_readlane_b32 s19, v49, 3
	v_readlane_b32 s20, v48, 4
	v_readlane_b32 s21, v49, 4
	v_readlane_b32 s22, v48, 5
	v_readlane_b32 s23, v49, 5
	v_readlane_b32 s24, v48, 6
	v_readlane_b32 s25, v49, 6
	v_readlane_b32 s26, v48, 7
	v_readlane_b32 s27, v49, 7
	s_waitcnt vmcnt(31)
	v_fmac_f32_e32 v92, s12, v60
	v_fmac_f32_e32 v93, s13, v60
	s_waitcnt vmcnt(30)
	v_fmac_f32_e32 v92, s14, v61
	v_fmac_f32_e32 v93, s15, v61
	s_waitcnt vmcnt(29)
	v_fmac_f32_e32 v92, s16, v62
	v_fmac_f32_e32 v93, s17, v62
	s_waitcnt vmcnt(28)
	v_fmac_f32_e32 v92, s18, v63
	v_fmac_f32_e32 v93, s19, v63
	s_waitcnt vmcnt(27)
	v_fmac_f32_e32 v92, s20, v64
	v_fmac_f32_e32 v93, s21, v64
	s_waitcnt vmcnt(26)
	v_fmac_f32_e32 v92, s22, v65
	v_fmac_f32_e32 v93, s23, v65
	s_waitcnt vmcnt(25)
	v_fmac_f32_e32 v92, s24, v66
	v_fmac_f32_e32 v93, s25, v66
	s_waitcnt vmcnt(24)
	v_fmac_f32_e32 v92, s26, v67
	v_fmac_f32_e32 v93, s27, v67
	v_readlane_b32 s12, v48, 8
	v_readlane_b32 s13, v49, 8
	v_readlane_b32 s14, v48, 9
	v_readlane_b32 s15, v49, 9
	v_readlane_b32 s16, v48, 10
	v_readlane_b32 s17, v49, 10
	v_readlane_b32 s18, v48, 11
	v_readlane_b32 s19, v49, 11
	v_readlane_b32 s20, v48, 12
	v_readlane_b32 s21, v49, 12
	v_readlane_b32 s22, v48, 13
	v_readlane_b32 s23, v49, 13
	v_readlane_b32 s24, v48, 14
	v_readlane_b32 s25, v49, 14
	v_readlane_b32 s26, v48, 15
	v_readlane_b32 s27, v49, 15
	s_waitcnt vmcnt(23)
	v_fmac_f32_e32 v92, s12, v68
	v_fmac_f32_e32 v93, s13, v68
	s_waitcnt vmcnt(22)
	v_fmac_f32_e32 v92, s14, v69
	v_fmac_f32_e32 v93, s15, v69
	s_waitcnt vmcnt(21)
	v_fmac_f32_e32 v92, s16, v70
	v_fmac_f32_e32 v93, s17, v70
	s_waitcnt vmcnt(20)
	v_fmac_f32_e32 v92, s18, v71
	v_fmac_f32_e32 v93, s19, v71
	s_waitcnt vmcnt(19)
	v_fmac_f32_e32 v92, s20, v72
	v_fmac_f32_e32 v93, s21, v72
	s_waitcnt vmcnt(18)
	v_fmac_f32_e32 v92, s22, v73
	v_fmac_f32_e32 v93, s23, v73
	s_waitcnt vmcnt(17)
	v_fmac_f32_e32 v92, s24, v74
	v_fmac_f32_e32 v93, s25, v74
	s_waitcnt vmcnt(16)
	v_fmac_f32_e32 v92, s26, v75
	v_fmac_f32_e32 v93, s27, v75
	global_load_dword v60, v46, s[28:29]
	global_load_dword v61, v46, s[28:29] offset:256
	global_load_dword v62, v46, s[28:29] offset:512
	global_load_dword v63, v46, s[28:29] offset:768
	global_load_dword v64, v46, s[28:29] offset:1024
	global_load_dword v65, v46, s[28:29] offset:1280
	global_load_dword v66, v46, s[28:29] offset:1536
	global_load_dword v67, v46, s[28:29] offset:1792
	global_load_dword v68, v46, s[28:29] offset:2048
	global_load_dword v69, v46, s[28:29] offset:2304
	global_load_dword v70, v46, s[28:29] offset:2560
	global_load_dword v71, v46, s[28:29] offset:2816
	global_load_dword v72, v46, s[28:29] offset:3072
	global_load_dword v73, v46, s[28:29] offset:3328
	global_load_dword v74, v46, s[28:29] offset:3584
	global_load_dword v75, v46, s[28:29] offset:3840
	s_add_u32 s28, s28, 0x1000
	s_addc_u32 s29, s29, 0
	v_readlane_b32 s12, v48, 16
	v_readlane_b32 s13, v49, 16
	v_readlane_b32 s14, v48, 17
	v_readlane_b32 s15, v49, 17
	v_readlane_b32 s16, v48, 18
	v_readlane_b32 s17, v49, 18
	v_readlane_b32 s18, v48, 19
	v_readlane_b32 s19, v49, 19
	v_readlane_b32 s20, v48, 20
	v_readlane_b32 s21, v49, 20
	v_readlane_b32 s22, v48, 21
	v_readlane_b32 s23, v49, 21
	v_readlane_b32 s24, v48, 22
	v_readlane_b32 s25, v49, 22
	v_readlane_b32 s26, v48, 23
	v_readlane_b32 s27, v49, 23
	s_waitcnt vmcnt(31)
	v_fmac_f32_e32 v92, s12, v76
	v_fmac_f32_e32 v93, s13, v76
	s_waitcnt vmcnt(30)
	v_fmac_f32_e32 v92, s14, v77
	v_fmac_f32_e32 v93, s15, v77
	s_waitcnt vmcnt(29)
	v_fmac_f32_e32 v92, s16, v78
	v_fmac_f32_e32 v93, s17, v78
	s_waitcnt vmcnt(28)
	v_fmac_f32_e32 v92, s18, v79
	v_fmac_f32_e32 v93, s19, v79
	s_waitcnt vmcnt(27)
	v_fmac_f32_e32 v92, s20, v80
	v_fmac_f32_e32 v93, s21, v80
	s_waitcnt vmcnt(26)
	v_fmac_f32_e32 v92, s22, v81
	v_fmac_f32_e32 v93, s23, v81
	s_waitcnt vmcnt(25)
	v_fmac_f32_e32 v92, s24, v82
	v_fmac_f32_e32 v93, s25, v82
	s_waitcnt vmcnt(24)
	v_fmac_f32_e32 v92, s26, v83
	v_fmac_f32_e32 v93, s27, v83
	v_readlane_b32 s12, v48, 24
	v_readlane_b32 s13, v49, 24
	v_readlane_b32 s14, v48, 25
	v_readlane_b32 s15, v49, 25
	v_readlane_b32 s16, v48, 26
	v_readlane_b32 s17, v49, 26
	v_readlane_b32 s18, v48, 27
	v_readlane_b32 s19, v49, 27
	v_readlane_b32 s20, v48, 28
	v_readlane_b32 s21, v49, 28
	v_readlane_b32 s22, v48, 29
	v_readlane_b32 s23, v49, 29
	v_readlane_b32 s24, v48, 30
	v_readlane_b32 s25, v49, 30
	v_readlane_b32 s26, v48, 31
	v_readlane_b32 s27, v49, 31
	s_waitcnt vmcnt(23)
	v_fmac_f32_e32 v92, s12, v84
	v_fmac_f32_e32 v93, s13, v84
	s_waitcnt vmcnt(22)
	v_fmac_f32_e32 v92, s14, v85
	v_fmac_f32_e32 v93, s15, v85
	s_waitcnt vmcnt(21)
	v_fmac_f32_e32 v92, s16, v86
	v_fmac_f32_e32 v93, s17, v86
	s_waitcnt vmcnt(20)
	v_fmac_f32_e32 v92, s18, v87
	v_fmac_f32_e32 v93, s19, v87
	s_waitcnt vmcnt(19)
	v_fmac_f32_e32 v92, s20, v88
	v_fmac_f32_e32 v93, s21, v88
	s_waitcnt vmcnt(18)
	v_fmac_f32_e32 v92, s22, v89
	v_fmac_f32_e32 v93, s23, v89
	s_waitcnt vmcnt(17)
	v_fmac_f32_e32 v92, s24, v90
	v_fmac_f32_e32 v93, s25, v90
	s_waitcnt vmcnt(16)
	v_fmac_f32_e32 v92, s26, v91
	v_fmac_f32_e32 v93, s27, v91
	global_load_dword v76, v46, s[28:29]
	global_load_dword v77, v46, s[28:29] offset:256
	global_load_dword v78, v46, s[28:29] offset:512
	global_load_dword v79, v46, s[28:29] offset:768
	global_load_dword v80, v46, s[28:29] offset:1024
	global_load_dword v81, v46, s[28:29] offset:1280
	global_load_dword v82, v46, s[28:29] offset:1536
	global_load_dword v83, v46, s[28:29] offset:1792
	global_load_dword v84, v46, s[28:29] offset:2048
	global_load_dword v85, v46, s[28:29] offset:2304
	global_load_dword v86, v46, s[28:29] offset:2560
	global_load_dword v87, v46, s[28:29] offset:2816
	global_load_dword v88, v46, s[28:29] offset:3072
	global_load_dword v89, v46, s[28:29] offset:3328
	global_load_dword v90, v46, s[28:29] offset:3584
	global_load_dword v91, v46, s[28:29] offset:3840
	v_readlane_b32 s12, v48, 32
	v_readlane_b32 s13, v49, 32
	v_readlane_b32 s14, v48, 33
	v_readlane_b32 s15, v49, 33
	v_readlane_b32 s16, v48, 34
	v_readlane_b32 s17, v49, 34
	v_readlane_b32 s18, v48, 35
	v_readlane_b32 s19, v49, 35
	v_readlane_b32 s20, v48, 36
	v_readlane_b32 s21, v49, 36
	v_readlane_b32 s22, v48, 37
	v_readlane_b32 s23, v49, 37
	v_readlane_b32 s24, v48, 38
	v_readlane_b32 s25, v49, 38
	v_readlane_b32 s26, v48, 39
	v_readlane_b32 s27, v49, 39
	s_waitcnt vmcnt(31)
	v_fmac_f32_e32 v92, s12, v60
	v_fmac_f32_e32 v93, s13, v60
	s_waitcnt vmcnt(30)
	v_fmac_f32_e32 v92, s14, v61
	v_fmac_f32_e32 v93, s15, v61
	s_waitcnt vmcnt(29)
	v_fmac_f32_e32 v92, s16, v62
	v_fmac_f32_e32 v93, s17, v62
	s_waitcnt vmcnt(28)
	v_fmac_f32_e32 v92, s18, v63
	v_fmac_f32_e32 v93, s19, v63
	s_waitcnt vmcnt(27)
	v_fmac_f32_e32 v92, s20, v64
	v_fmac_f32_e32 v93, s21, v64
	s_waitcnt vmcnt(26)
	v_fmac_f32_e32 v92, s22, v65
	v_fmac_f32_e32 v93, s23, v65
	s_waitcnt vmcnt(25)
	v_fmac_f32_e32 v92, s24, v66
	v_fmac_f32_e32 v93, s25, v66
	s_waitcnt vmcnt(24)
	v_fmac_f32_e32 v92, s26, v67
	v_fmac_f32_e32 v93, s27, v67
	v_readlane_b32 s12, v48, 40
	v_readlane_b32 s13, v49, 40
	v_readlane_b32 s14, v48, 41
	v_readlane_b32 s15, v49, 41
	v_readlane_b32 s16, v48, 42
	v_readlane_b32 s17, v49, 42
	v_readlane_b32 s18, v48, 43
	v_readlane_b32 s19, v49, 43
	v_readlane_b32 s20, v48, 44
	v_readlane_b32 s21, v49, 44
	v_readlane_b32 s22, v48, 45
	v_readlane_b32 s23, v49, 45
	v_readlane_b32 s24, v48, 46
	v_readlane_b32 s25, v49, 46
	v_readlane_b32 s26, v48, 47
	v_readlane_b32 s27, v49, 47
	s_waitcnt vmcnt(23)
	v_fmac_f32_e32 v92, s12, v68
	v_fmac_f32_e32 v93, s13, v68
	s_waitcnt vmcnt(22)
	v_fmac_f32_e32 v92, s14, v69
	v_fmac_f32_e32 v93, s15, v69
	s_waitcnt vmcnt(21)
	v_fmac_f32_e32 v92, s16, v70
	v_fmac_f32_e32 v93, s17, v70
	s_waitcnt vmcnt(20)
	v_fmac_f32_e32 v92, s18, v71
	v_fmac_f32_e32 v93, s19, v71
	s_waitcnt vmcnt(19)
	v_fmac_f32_e32 v92, s20, v72
	v_fmac_f32_e32 v93, s21, v72
	s_waitcnt vmcnt(18)
	v_fmac_f32_e32 v92, s22, v73
	v_fmac_f32_e32 v93, s23, v73
	s_waitcnt vmcnt(17)
	v_fmac_f32_e32 v92, s24, v74
	v_fmac_f32_e32 v93, s25, v74
	s_waitcnt vmcnt(16)
	v_fmac_f32_e32 v92, s26, v75
	v_fmac_f32_e32 v93, s27, v75
	v_readlane_b32 s12, v48, 48
	v_readlane_b32 s13, v49, 48
	v_readlane_b32 s14, v48, 49
	v_readlane_b32 s15, v49, 49
	v_readlane_b32 s16, v48, 50
	v_readlane_b32 s17, v49, 50
	v_readlane_b32 s18, v48, 51
	v_readlane_b32 s19, v49, 51
	v_readlane_b32 s20, v48, 52
	v_readlane_b32 s21, v49, 52
	v_readlane_b32 s22, v48, 53
	v_readlane_b32 s23, v49, 53
	v_readlane_b32 s24, v48, 54
	v_readlane_b32 s25, v49, 54
	v_readlane_b32 s26, v48, 55
	v_readlane_b32 s27, v49, 55
	s_waitcnt vmcnt(15)
	v_fmac_f32_e32 v92, s12, v76
	v_fmac_f32_e32 v93, s13, v76
	s_waitcnt vmcnt(14)
	v_fmac_f32_e32 v92, s14, v77
	v_fmac_f32_e32 v93, s15, v77
	s_waitcnt vmcnt(13)
	v_fmac_f32_e32 v92, s16, v78
	v_fmac_f32_e32 v93, s17, v78
	s_waitcnt vmcnt(12)
	v_fmac_f32_e32 v92, s18, v79
	v_fmac_f32_e32 v93, s19, v79
	s_waitcnt vmcnt(11)
	v_fmac_f32_e32 v92, s20, v80
	v_fmac_f32_e32 v93, s21, v80
	s_waitcnt vmcnt(10)
	v_fmac_f32_e32 v92, s22, v81
	v_fmac_f32_e32 v93, s23, v81
	s_waitcnt vmcnt(9)
	v_fmac_f32_e32 v92, s24, v82
	v_fmac_f32_e32 v93, s25, v82
	s_waitcnt vmcnt(8)
	v_fmac_f32_e32 v92, s26, v83
	v_fmac_f32_e32 v93, s27, v83
	v_readlane_b32 s12, v48, 56
	v_readlane_b32 s13, v49, 56
	v_readlane_b32 s14, v48, 57
	v_readlane_b32 s15, v49, 57
	v_readlane_b32 s16, v48, 58
	v_readlane_b32 s17, v49, 58
	v_readlane_b32 s18, v48, 59
	v_readlane_b32 s19, v49, 59
	v_readlane_b32 s20, v48, 60
	v_readlane_b32 s21, v49, 60
	v_readlane_b32 s22, v48, 61
	v_readlane_b32 s23, v49, 61
	v_readlane_b32 s24, v48, 62
	v_readlane_b32 s25, v49, 62
	v_readlane_b32 s26, v48, 63
	v_readlane_b32 s27, v49, 63
	s_waitcnt vmcnt(7)
	v_fmac_f32_e32 v92, s12, v84
	v_fmac_f32_e32 v93, s13, v84
	s_waitcnt vmcnt(6)
	v_fmac_f32_e32 v92, s14, v85
	v_fmac_f32_e32 v93, s15, v85
	s_waitcnt vmcnt(5)
	v_fmac_f32_e32 v92, s16, v86
	v_fmac_f32_e32 v93, s17, v86
	s_waitcnt vmcnt(4)
	v_fmac_f32_e32 v92, s18, v87
	v_fmac_f32_e32 v93, s19, v87
	s_waitcnt vmcnt(3)
	v_fmac_f32_e32 v92, s20, v88
	v_fmac_f32_e32 v93, s21, v88
	s_waitcnt vmcnt(2)
	v_fmac_f32_e32 v92, s22, v89
	v_fmac_f32_e32 v93, s23, v89
	s_waitcnt vmcnt(1)
	v_fmac_f32_e32 v92, s24, v90
	v_fmac_f32_e32 v93, s25, v90
	s_waitcnt vmcnt(0)
	v_fmac_f32_e32 v92, s26, v91
	v_fmac_f32_e32 v93, s27, v91
	v_lshlrev_b32_e32 v58, 9, v53
	v_cmp_lt_i32_e32 vcc, v52, v57
	v_or_b32_e32 v1, 0x800, v58
	v_or_b32_e32 v2, v1, v46
	s_waitcnt vmcnt(0)
	v_cndmask_b32_e32 v0, v44, v24, vcc
	ds_write2st64_b32 v2, v0, v50 offset1:1
	v_lshlrev_b32_e32 v50, 2, v55
	v_or_b32_e32 v26, v1, v50
	ds_read2_b32 v[0:1], v26 offset1:4
	ds_read2_b32 v[20:21], v26 offset0:16 offset1:20
	v_lshl_or_b32 v45, v47, 4, v8
	v_cndmask_b32_e32 v59, 0, v25, vcc
	ds_read2_b32 v[24:25], v26 offset0:24 offset1:28
	s_waitcnt lgkmcnt(2)
	v_lshl_add_u32 v0, v0, 7, v45
	s_waitcnt lgkmcnt(1)
	v_lshl_add_u32 v16, v20, 7, v45
	global_load_dwordx4 v[8:11], v0, s[4:5]
	v_lshl_add_u32 v20, v21, 7, v45
	global_load_dwordx4 v[16:19], v16, s[4:5]
	v_lshl_add_u32 v0, v1, 7, v45
	global_load_dwordx4 v[12:15], v0, s[4:5]
	v_or_b32_e32 v27, 0x1000, v58
	global_load_dwordx4 v[20:23], v20, s[4:5]
	ds_read2_b32 v[0:1], v26 offset0:8 offset1:12
	s_waitcnt lgkmcnt(1)
	v_lshl_add_u32 v24, v24, 7, v45
	v_or_b32_e32 v30, v27, v46
	v_or_b32_e32 v60, v27, v50
	s_mov_b32 s3, 48
	s_waitcnt lgkmcnt(0)
	v_lshl_add_u32 v0, v0, 7, v45
	global_load_dwordx4 v[4:7], v0, s[4:5]
	v_lshl_add_u32 v0, v1, 7, v45
	global_load_dwordx4 v[0:3], v0, s[4:5]
	ds_read2_b32 v[28:29], v26 offset0:32 offset1:36
	ds_read2_b32 v[26:27], v26 offset0:40 offset1:44
	global_load_dwordx4 v[40:43], v24, s[4:5]
	ds_write2st64_b32 v30, v59, v51 offset1:1
	v_lshl_add_u32 v24, v25, 7, v45
	s_waitcnt lgkmcnt(2)
	v_lshl_add_u32 v25, v28, 7, v45
	v_lshl_add_u32 v28, v29, 7, v45
	s_waitcnt lgkmcnt(1)
	v_lshl_add_u32 v26, v26, 7, v45
	v_lshl_add_u32 v27, v27, 7, v45
	global_load_dwordx4 v[62:65], v24, s[4:5]
	global_load_dwordx4 v[36:39], v25, s[4:5]
	global_load_dwordx4 v[32:35], v28, s[4:5]
	s_nop 0
	global_load_dwordx4 v[28:31], v26, s[4:5]
	s_nop 0
	global_load_dwordx4 v[24:27], v27, s[4:5]
	v_cmp_lt_i32_e32 vcc, 48, v57
	s_waitcnt vmcnt(11)
	v_cvt_f32_f16_e32 v70, v10
	v_cvt_f32_f16_sdwa v71, v10 dst_sel:DWORD dst_unused:UNUSED_PAD src0_sel:WORD_1
	v_cvt_f32_f16_e32 v66, v8
	v_cvt_f32_f16_sdwa v67, v8 dst_sel:DWORD dst_unused:UNUSED_PAD src0_sel:WORD_1
	s_waitcnt vmcnt(9)
	v_cvt_f32_f16_e32 v74, v14
	v_cvt_f32_f16_sdwa v75, v14 dst_sel:DWORD dst_unused:UNUSED_PAD src0_sel:WORD_1
	s_waitcnt vmcnt(8)
	v_cvt_f32_f16_e32 v84, v22
	v_cvt_f32_f16_sdwa v85, v22 dst_sel:DWORD dst_unused:UNUSED_PAD src0_sel:WORD_1
	v_cvt_f32_f16_e32 v91, v23
	v_cvt_f32_f16_e32 v87, v15
	v_cvt_f32_f16_e32 v68, v9
	v_cvt_f32_f16_sdwa v69, v9 dst_sel:DWORD dst_unused:UNUSED_PAD src0_sel:WORD_1
	v_cvt_f32_f16_e32 v72, v12
	v_cvt_f32_f16_sdwa v73, v12 dst_sel:DWORD dst_unused:UNUSED_PAD src0_sel:WORD_1
	v_cvt_f32_f16_e32 v12, v13
	s_waitcnt vmcnt(6)
	v_cvt_f32_f16_e32 v78, v1
	v_cvt_f32_f16_sdwa v79, v1 dst_sel:DWORD dst_unused:UNUSED_PAD src0_sel:WORD_1
	v_cvt_f32_f16_sdwa v1, v23 dst_sel:DWORD dst_unused:UNUSED_PAD src0_sel:WORD_1
	ds_read2_b32 v[22:23], v60 offset1:4
	v_cvt_f32_f16_sdwa v13, v13 dst_sel:DWORD dst_unused:UNUSED_PAD src0_sel:WORD_1
	v_cvt_f32_f16_e32 v61, v11
	v_cvt_f32_f16_sdwa v9, v15 dst_sel:DWORD dst_unused:UNUSED_PAD src0_sel:WORD_1
	v_cvt_f32_f16_sdwa v8, v11 dst_sel:DWORD dst_unused:UNUSED_PAD src0_sel:WORD_1
	s_waitcnt lgkmcnt(0)
	v_mov_b32_e32 v86, v23
	v_pk_fma_f32 v[70:71], v[22:23], v[70:71], 0 op_sel_hi:[0,1,0]
	v_pk_fma_f32 v[70:71], v[86:87], v[74:75], v[70:71] op_sel_hi:[0,1,1]
	ds_read2_b32 v[74:75], v60 offset0:8 offset1:12
	v_cvt_f32_f16_e32 v10, v4
	v_cvt_f32_f16_sdwa v11, v4 dst_sel:DWORD dst_unused:UNUSED_PAD src0_sel:WORD_1
	v_cvt_f32_f16_e32 v14, v5
	v_cvt_f32_f16_sdwa v15, v5 dst_sel:DWORD dst_unused:UNUSED_PAD src0_sel:WORD_1
	v_cvt_f32_f16_e32 v76, v6
	v_cvt_f32_f16_sdwa v77, v6 dst_sel:DWORD dst_unused:UNUSED_PAD src0_sel:WORD_1
	v_cvt_f32_f16_e32 v88, v7
	v_cvt_f32_f16_sdwa v4, v7 dst_sel:DWORD dst_unused:UNUSED_PAD src0_sel:WORD_1
	v_cvt_f32_f16_e32 v6, v0
	v_cvt_f32_f16_sdwa v7, v0 dst_sel:DWORD dst_unused:UNUSED_PAD src0_sel:WORD_1
	v_cvt_f32_f16_e32 v80, v2
	v_cvt_f32_f16_sdwa v81, v2 dst_sel:DWORD dst_unused:UNUSED_PAD src0_sel:WORD_1
	v_pk_fma_f32 v[68:69], v[22:23], v[68:69], 0 op_sel_hi:[0,1,0]
	v_pk_fma_f32 v[66:67], v[22:23], v[66:67], 0 op_sel_hi:[0,1,0]
	v_pk_fma_f32 v[12:13], v[86:87], v[12:13], v[68:69] op_sel_hi:[0,1,1]
	v_pk_fma_f32 v[66:67], v[86:87], v[72:73], v[66:67] op_sel_hi:[0,1,1]
	s_waitcnt lgkmcnt(0)
	v_pk_fma_f32 v[10:11], v[74:75], v[10:11], v[66:67] op_sel_hi:[0,1,1]
	v_pk_fma_f32 v[12:13], v[74:75], v[14:15], v[12:13] op_sel_hi:[0,1,1]
	v_mov_b32_e32 v14, v75
	v_pk_fma_f32 v[66:67], v[74:75], v[76:77], v[70:71] op_sel_hi:[0,1,1]
	v_pk_fma_f32 v[66:67], v[14:15], v[80:81], v[66:67] op_sel_hi:[0,1,1]
	v_pk_fma_f32 v[12:13], v[14:15], v[78:79], v[12:13] op_sel_hi:[0,1,1]
	v_pk_fma_f32 v[6:7], v[14:15], v[6:7], v[10:11] op_sel_hi:[0,1,1]
	s_waitcnt vmcnt(5)
	v_cvt_f32_f16_e32 v10, v40
	v_cvt_f32_f16_sdwa v11, v40 dst_sel:DWORD dst_unused:UNUSED_PAD src0_sel:WORD_1
	v_cvt_f32_f16_e32 v14, v41
	v_cvt_f32_f16_sdwa v15, v41 dst_sel:DWORD dst_unused:UNUSED_PAD src0_sel:WORD_1
	ds_read2_b32 v[40:41], v60 offset0:16 offset1:20
	v_cvt_f32_f16_e32 v89, v3
	v_cvt_f32_f16_sdwa v5, v3 dst_sel:DWORD dst_unused:UNUSED_PAD src0_sel:WORD_1
	v_cvt_f32_f16_e32 v2, v16
	v_cvt_f32_f16_sdwa v3, v16 dst_sel:DWORD dst_unused:UNUSED_PAD src0_sel:WORD_1
	v_cvt_f32_f16_e32 v16, v17
	v_cvt_f32_f16_sdwa v17, v17 dst_sel:DWORD dst_unused:UNUSED_PAD src0_sel:WORD_1
	v_cvt_f32_f16_e32 v90, v19
	v_cvt_f32_f16_e32 v82, v18
	v_cvt_f32_f16_sdwa v83, v18 dst_sel:DWORD dst_unused:UNUSED_PAD src0_sel:WORD_1
	v_cvt_f32_f16_sdwa v0, v19 dst_sel:DWORD dst_unused:UNUSED_PAD src0_sel:WORD_1
	v_cvt_f32_f16_e32 v18, v20
	v_cvt_f32_f16_sdwa v19, v20 dst_sel:DWORD dst_unused:UNUSED_PAD src0_sel:WORD_1
	v_cvt_f32_f16_e32 v20, v21
	v_cvt_f32_f16_sdwa v21, v21 dst_sel:DWORD dst_unused:UNUSED_PAD src0_sel:WORD_1
	s_waitcnt lgkmcnt(0)
	v_pk_fma_f32 v[2:3], v[40:41], v[2:3], v[6:7] op_sel_hi:[0,1,1]
	v_pk_fma_f32 v[6:7], v[40:41], v[16:17], v[12:13] op_sel_hi:[0,1,1]
	v_mov_b32_e32 v16, v41
	v_pk_fma_f32 v[2:3], v[16:17], v[18:19], v[2:3] op_sel_hi:[0,1,1]
	ds_read2_b32 v[18:19], v60 offset0:24 offset1:28
	v_cvt_f32_f16_e32 v68, v42
	v_cvt_f32_f16_sdwa v69, v42 dst_sel:DWORD dst_unused:UNUSED_PAD src0_sel:WORD_1
	v_pk_fma_f32 v[12:13], v[40:41], v[82:83], v[66:67] op_sel_hi:[0,1,1]
	v_pk_fma_f32 v[12:13], v[16:17], v[84:85], v[12:13] op_sel_hi:[0,1,1]
	v_pk_fma_f32 v[6:7], v[16:17], v[20:21], v[6:7] op_sel_hi:[0,1,1]
	s_waitcnt vmcnt(4)
	v_cvt_f32_f16_e32 v20, v62
	v_cvt_f32_f16_sdwa v21, v62 dst_sel:DWORD dst_unused:UNUSED_PAD src0_sel:WORD_1
	v_cvt_f32_f16_e32 v16, v63
	v_cvt_f32_f16_sdwa v17, v63 dst_sel:DWORD dst_unused:UNUSED_PAD src0_sel:WORD_1
	v_cvt_f32_f16_e32 v62, v64
	v_cvt_f32_f16_sdwa v63, v64 dst_sel:DWORD dst_unused:UNUSED_PAD src0_sel:WORD_1
	v_pk_mul_f32 v[8:9], v[22:23], v[8:9]
	s_waitcnt lgkmcnt(0)
	v_pk_fma_f32 v[2:3], v[18:19], v[10:11], v[2:3] op_sel_hi:[0,1,1]
	v_pk_fma_f32 v[10:11], v[18:19], v[68:69], v[12:13] op_sel_hi:[0,1,1]
	v_mov_b32_e32 v12, v19
	s_waitcnt vmcnt(0)
	v_cvt_f32_f16_e32 v66, v26
	v_cvt_f32_f16_sdwa v67, v26 dst_sel:DWORD dst_unused:UNUSED_PAD src0_sel:WORD_1
	v_mul_f32_e32 v22, v22, v61
	v_mul_f32_e32 v26, v23, v87
	v_mov_b32_e32 v23, v8
	v_pk_fma_f32 v[10:11], v[12:13], v[62:63], v[10:11] op_sel_hi:[0,1,1]
	v_cvt_f32_f16_e32 v62, v30
	v_cvt_f32_f16_sdwa v63, v30 dst_sel:DWORD dst_unused:UNUSED_PAD src0_sel:WORD_1
	v_cvt_f32_f16_e32 v72, v31
	v_cvt_f32_f16_sdwa v30, v31 dst_sel:DWORD dst_unused:UNUSED_PAD src0_sel:WORD_1
	v_cvt_f32_f16_sdwa v31, v27 dst_sel:DWORD dst_unused:UNUSED_PAD src0_sel:WORD_1
	v_cvt_f32_f16_e32 v73, v27
	v_mov_b32_e32 v27, v9
	v_pk_add_f32 v[8:9], v[22:23], 0 op_sel_hi:[1,0]
	v_pk_mul_f32 v[4:5], v[74:75], v[4:5]
	v_pk_add_f32 v[8:9], v[8:9], v[26:27]
	v_mul_f32_e32 v22, v74, v88
	v_mov_b32_e32 v23, v4
	v_pk_add_f32 v[8:9], v[8:9], v[22:23]
	v_mul_f32_e32 v4, v75, v89
	v_pk_mul_f32 v[0:1], v[40:41], v[0:1]
	v_pk_add_f32 v[4:5], v[8:9], v[4:5]
	v_mul_f32_e32 v8, v40, v90
	v_mov_b32_e32 v9, v0
	v_pk_add_f32 v[4:5], v[4:5], v[8:9]
	v_mul_f32_e32 v0, v41, v91
	v_pk_fma_f32 v[6:7], v[18:19], v[14:15], v[6:7] op_sel_hi:[0,1,1]
	v_pk_add_f32 v[0:1], v[4:5], v[0:1]
	ds_read2_b32 v[4:5], v60 offset0:32 offset1:36
	v_pk_fma_f32 v[6:7], v[12:13], v[16:17], v[6:7] op_sel_hi:[0,1,1]
	v_pk_fma_f32 v[2:3], v[12:13], v[20:21], v[2:3] op_sel_hi:[0,1,1]
	v_cvt_f32_f16_e32 v12, v36
	v_cvt_f32_f16_sdwa v13, v36 dst_sel:DWORD dst_unused:UNUSED_PAD src0_sel:WORD_1
	v_cvt_f32_f16_e32 v70, v43
	v_cvt_f32_f16_sdwa v42, v43 dst_sel:DWORD dst_unused:UNUSED_PAD src0_sel:WORD_1
	v_cvt_f32_f16_sdwa v43, v65 dst_sel:DWORD dst_unused:UNUSED_PAD src0_sel:WORD_1
	v_cvt_f32_f16_e32 v71, v65
	v_cvt_f32_f16_sdwa v20, v39 dst_sel:DWORD dst_unused:UNUSED_PAD src0_sel:WORD_1
	v_cvt_f32_f16_sdwa v21, v35 dst_sel:DWORD dst_unused:UNUSED_PAD src0_sel:WORD_1
	v_cvt_f32_f16_e32 v14, v37
	v_cvt_f32_f16_sdwa v15, v37 dst_sel:DWORD dst_unused:UNUSED_PAD src0_sel:WORD_1
	v_cvt_f32_f16_e32 v68, v39
	s_waitcnt lgkmcnt(0)
	v_pk_fma_f32 v[2:3], v[4:5], v[12:13], v[2:3] op_sel_hi:[0,1,1]
	ds_read2_b32 v[12:13], v60 offset0:40 offset1:44
	v_cvt_f32_f16_e32 v16, v38
	v_cvt_f32_f16_sdwa v17, v38 dst_sel:DWORD dst_unused:UNUSED_PAD src0_sel:WORD_1
	v_cvt_f32_f16_e32 v69, v35
	v_pk_mul_f32 v[8:9], v[18:19], v[42:43]
	v_cvt_f32_f16_e32 v36, v32
	v_cvt_f32_f16_sdwa v37, v32 dst_sel:DWORD dst_unused:UNUSED_PAD src0_sel:WORD_1
	v_cvt_f32_f16_e32 v32, v33
	v_cvt_f32_f16_sdwa v33, v33 dst_sel:DWORD dst_unused:UNUSED_PAD src0_sel:WORD_1
	v_cvt_f32_f16_e32 v38, v34
	v_cvt_f32_f16_sdwa v39, v34 dst_sel:DWORD dst_unused:UNUSED_PAD src0_sel:WORD_1
	v_mul_f32_e32 v22, v18, v70
	v_mov_b32_e32 v23, v8
	v_cvt_f32_f16_e32 v34, v28
	v_cvt_f32_f16_sdwa v35, v28 dst_sel:DWORD dst_unused:UNUSED_PAD src0_sel:WORD_1
	v_cvt_f32_f16_e32 v28, v29
	v_cvt_f32_f16_sdwa v29, v29 dst_sel:DWORD dst_unused:UNUSED_PAD src0_sel:WORD_1
	v_pk_add_f32 v[0:1], v[0:1], v[22:23]
	v_mul_f32_e32 v8, v19, v71
	v_pk_mul_f32 v[18:19], v[4:5], v[20:21]
	v_cvt_f32_f16_e32 v64, v24
	v_cvt_f32_f16_sdwa v65, v24 dst_sel:DWORD dst_unused:UNUSED_PAD src0_sel:WORD_1
	v_cvt_f32_f16_e32 v24, v25
	v_cvt_f32_f16_sdwa v25, v25 dst_sel:DWORD dst_unused:UNUSED_PAD src0_sel:WORD_1
	v_pk_fma_f32 v[6:7], v[4:5], v[14:15], v[6:7] op_sel_hi:[0,1,1]
	v_mul_f32_e32 v14, v4, v68
	v_pk_add_f32 v[0:1], v[0:1], v[8:9]
	v_mov_b32_e32 v15, v18
	v_pk_fma_f32 v[10:11], v[4:5], v[16:17], v[10:11] op_sel_hi:[0,1,1]
	v_mul_f32_e32 v16, v5, v69
	v_mov_b32_e32 v20, v5
	s_waitcnt lgkmcnt(0)
	v_pk_mul_f32 v[26:27], v[12:13], v[30:31]
	v_pk_add_f32 v[0:1], v[0:1], v[14:15]
	v_mov_b32_e32 v17, v19
	v_mul_f32_e32 v4, v12, v72
	v_pk_fma_f32 v[10:11], v[20:21], v[38:39], v[10:11] op_sel_hi:[0,1,1]
	v_pk_fma_f32 v[6:7], v[20:21], v[32:33], v[6:7] op_sel_hi:[0,1,1]
	v_pk_fma_f32 v[2:3], v[20:21], v[36:37], v[2:3] op_sel_hi:[0,1,1]
	v_pk_add_f32 v[0:1], v[0:1], v[16:17]
	v_mov_b32_e32 v5, v26
	v_mov_b32_e32 v22, v13
	v_mul_f32_e32 v8, v13, v73
	v_pk_add_f32 v[14:15], v[0:1], v[4:5]
	v_pk_fma_f32 v[0:1], v[12:13], v[34:35], v[2:3] op_sel_hi:[0,1,1]
	v_pk_fma_f32 v[2:3], v[12:13], v[28:29], v[6:7] op_sel_hi:[0,1,1]
	v_pk_fma_f32 v[4:5], v[12:13], v[62:63], v[10:11] op_sel_hi:[0,1,1]
	v_mov_b32_e32 v9, v27
	v_pk_fma_f32 v[4:5], v[22:23], v[66:67], v[4:5] op_sel_hi:[0,1,1]
	v_pk_fma_f32 v[2:3], v[22:23], v[24:25], v[2:3] op_sel_hi:[0,1,1]
	v_pk_fma_f32 v[0:1], v[22:23], v[64:65], v[0:1] op_sel_hi:[0,1,1]
	v_pk_add_f32 v[6:7], v[14:15], v[8:9]
	s_and_saveexec_b64 s[8:9], vcc
	s_cbranch_execz .LBB4_17
	s_movk_i32 s10, 0x8c0
	v_or3_b32 v24, v58, v50, s10
	s_mov_b64 s[10:11], 0

.LBB4_20:
	s_or_b64 exec, exec, s[10:11]
	v_lshlrev_b32_e32 v21, 9, v53
	v_lshl_add_u32 v21, v52, 2, v21
	ds_read_b32 v46, v21
	ds_read_b32 v47, v21 offset:256
	v_mov_b32_e32 v48, v92
	v_mov_b32_e32 v49, v93
	s_waitcnt lgkmcnt(0)
	v_mov_b32_e32 v0, v49
	v_mov_b32_e32 v1, v48
	v_pk_mul_f32 v[2:3], v[48:49], v[46:47] op_sel_hi:[1,0]
	v_pk_mul_f32 v[4:5], v[0:1], v[46:47] op_sel:[0,1]
	ds_bpermute_b32 v2, v19, v2
	ds_bpermute_b32 v3, v19, v3
	ds_bpermute_b32 v4, v19, v4
	ds_bpermute_b32 v5, v19, v5
	v_cmp_eq_u32_e32 vcc, 0, v52
	s_waitcnt lgkmcnt(2)
	v_pk_fma_f32 v[2:3], v[48:49], v[46:47], v[2:3] op_sel_hi:[1,0,1]
	ds_bpermute_b32 v6, v15, v2
	s_waitcnt lgkmcnt(1)
	v_pk_fma_f32 v[0:1], v[0:1], v[46:47], v[4:5] op_sel:[0,1,0]
	ds_bpermute_b32 v7, v15, v3
	ds_bpermute_b32 v4, v15, v0
	ds_bpermute_b32 v5, v15, v1
	s_waitcnt lgkmcnt(2)
	v_pk_add_f32 v[2:3], v[2:3], v[6:7]
	ds_bpermute_b32 v6, v13, v2
	s_waitcnt lgkmcnt(1)
	v_pk_add_f32 v[0:1], v[0:1], v[4:5]
	ds_bpermute_b32 v7, v13, v3
	ds_bpermute_b32 v4, v13, v0
	ds_bpermute_b32 v5, v13, v1
	s_waitcnt lgkmcnt(2)
	v_pk_add_f32 v[2:3], v[2:3], v[6:7]
	ds_bpermute_b32 v6, v11, v2
	s_waitcnt lgkmcnt(1)
	v_pk_add_f32 v[0:1], v[0:1], v[4:5]
	ds_bpermute_b32 v7, v11, v3
	ds_bpermute_b32 v4, v11, v0
	ds_bpermute_b32 v5, v11, v1
	s_waitcnt lgkmcnt(2)
	v_pk_add_f32 v[2:3], v[2:3], v[6:7]
	ds_bpermute_b32 v6, v9, v2
	s_waitcnt lgkmcnt(1)
	v_pk_add_f32 v[0:1], v[0:1], v[4:5]
	ds_bpermute_b32 v7, v9, v3
	ds_bpermute_b32 v4, v9, v0
	ds_bpermute_b32 v5, v9, v1
	s_waitcnt lgkmcnt(2)
	v_pk_add_f32 v[2:3], v[2:3], v[6:7]
	ds_bpermute_b32 v6, v17, v2
	s_waitcnt lgkmcnt(1)
	v_pk_add_f32 v[0:1], v[0:1], v[4:5]
	ds_bpermute_b32 v7, v17, v3
	ds_bpermute_b32 v4, v17, v0
	ds_bpermute_b32 v5, v17, v1
	s_and_saveexec_b64 s[0:1], vcc
	s_cbranch_execz .LBB4_24
	v_lshlrev_b32_e32 v8, 1, v44
	v_ashrrev_i32_e32 v9, 31, v8
	v_lshlrev_b64 v[8:9], 2, v[8:9]
	s_waitcnt lgkmcnt(2)
	v_pk_add_f32 v[2:3], v[2:3], v[6:7]
	v_lshl_add_u64 v[10:11], s[4:5], 0, v[8:9]
	v_pk_add_f32 v[2:3], s[2:3], v[2:3] op_sel_hi:[0,1]
	s_waitcnt lgkmcnt(0)
	v_pk_add_f32 v[0:1], v[0:1], v[4:5]
	global_store_dwordx2 v[10:11], v[2:3], off
	v_lshl_add_u64 v[2:3], s[6:7], 0, v[8:9]
	v_pk_add_f32 v[0:1], s[2:3], v[0:1] op_sel_hi:[0,1]
	global_store_dwordx2 v[2:3], v[0:1], off

	.amdhsa_kernel _Z9k_readoutPKDv4_jPKfPKiPK15HIP_vector_typeIiLj2EES3_S3_S3_PfSA_
		.amdhsa_group_segment_fixed_size 6144
		.amdhsa_private_segment_fixed_size 0
		.amdhsa_kernarg_size 72
		.amdhsa_user_sgpr_count 2
		.amdhsa_user_sgpr_dispatch_ptr 0
		.amdhsa_user_sgpr_queue_ptr 0
		.amdhsa_user_sgpr_kernarg_segment_ptr 1
		.amdhsa_user_sgpr_dispatch_id 0
		.amdhsa_user_sgpr_kernarg_preload_length 0
		.amdhsa_user_sgpr_kernarg_preload_offset 0
		.amdhsa_user_sgpr_private_segment_size 0
		.amdhsa_uses_dynamic_stack 0
		.amdhsa_enable_private_segment 0
		.amdhsa_system_sgpr_workgroup_id_x 1
		.amdhsa_system_sgpr_workgroup_id_y 0
		.amdhsa_system_sgpr_workgroup_id_z 0
		.amdhsa_system_sgpr_workgroup_info 0
		.amdhsa_system_vgpr_workitem_id 0
		.amdhsa_next_free_vgpr 94
		.amdhsa_next_free_sgpr 30
		.amdhsa_accum_offset 96
		.amdhsa_reserve_vcc 1
		.amdhsa_float_round_mode_32 0
		.amdhsa_float_round_mode_16_64 0
		.amdhsa_float_denorm_mode_32 3
		.amdhsa_float_denorm_mode_16_64 3
		.amdhsa_dx10_clamp 1
		.amdhsa_ieee_mode 1
		.amdhsa_fp16_overflow 0
		.amdhsa_tg_split 0
		.amdhsa_exception_fp_ieee_invalid_op 0
		.amdhsa_exception_fp_denorm_src 0
		.amdhsa_exception_fp_ieee_div_zero 0
		.amdhsa_exception_fp_ieee_overflow 0
		.amdhsa_exception_fp_ieee_underflow 0
		.amdhsa_exception_fp_ieee_inexact 0
		.amdhsa_exception_int_div_zero 0
	.end_amdhsa_kernel

amdhsa.kernels:
  - .agpr_count:     0
    .args:
      - .actual_access:  read_only
        .address_space:  global
        .offset:         0
        .size:           8
        .value_kind:     global_buffer
      - .actual_access:  read_only
        .address_space:  global
        .offset:         8
        .size:           8
        .value_kind:     global_buffer
      - .actual_access:  read_only
        .address_space:  global
        .offset:         16
        .size:           8
        .value_kind:     global_buffer
      - .actual_access:  write_only
        .address_space:  global
        .offset:         24
        .size:           8
        .value_kind:     global_buffer
      - .actual_access:  write_only
        .address_space:  global
        .offset:         32
        .size:           8
        .value_kind:     global_buffer
      - .actual_access:  write_only
        .address_space:  global
        .offset:         40
        .size:           8
        .value_kind:     global_buffer
      - .actual_access:  read_only
        .address_space:  global
        .offset:         48
        .size:           8
        .value_kind:     global_buffer
      - .actual_access:  read_only
        .address_space:  global
        .offset:         56
        .size:           8
        .value_kind:     global_buffer
      - .actual_access:  read_only
        .address_space:  global
        .offset:         64
        .size:           8
        .value_kind:     global_buffer
      - .actual_access:  write_only
        .address_space:  global
        .offset:         72
        .size:           8
        .value_kind:     global_buffer
    .group_segment_fixed_size: 0
    .kernarg_segment_align: 8
    .kernarg_segment_size: 80
    .language:       OpenCL C
    .language_version:
      - 2
      - 0
    .max_flat_workgroup_size: 256
    .name:           _Z8k_phase1PKfS0_S0_PDv4_jS2_PiS3_P15HIP_vector_typeIiLj2EES0_Pf
    .private_segment_fixed_size: 0
    .sgpr_count:     18
    .sgpr_spill_count: 0
    .symbol:         _Z8k_phase1PKfS0_S0_PDv4_jS2_PiS3_P15HIP_vector_typeIiLj2EES0_Pf.kd
    .uniform_work_group_size: 1
    .uses_dynamic_stack: false
    .vgpr_count:     19
    .vgpr_spill_count: 0
    .wavefront_size: 64
  - .agpr_count:     0
    .args:
      - .actual_access:  read_only
        .address_space:  global
        .offset:         0
        .size:           8
        .value_kind:     global_buffer
      - .actual_access:  read_only
        .address_space:  global
        .offset:         8
        .size:           8
        .value_kind:     global_buffer
      - .actual_access:  read_only
        .address_space:  global
        .offset:         16
        .size:           8
        .value_kind:     global_buffer
      - .actual_access:  read_only
        .address_space:  global
        .offset:         24
        .size:           8
        .value_kind:     global_buffer
      - .address_space:  global
        .offset:         32
        .size:           8
        .value_kind:     global_buffer
      - .actual_access:  write_only
        .address_space:  global
        .offset:         40
        .size:           8
        .value_kind:     global_buffer
      - .actual_access:  write_only
        .address_space:  global
        .offset:         48
        .size:           8
        .value_kind:     global_buffer
      - .actual_access:  write_only
        .address_space:  global
        .offset:         56
        .size:           8
        .value_kind:     global_buffer
      - .actual_access:  read_only
        .address_space:  global
        .offset:         64
        .size:           8
        .value_kind:     global_buffer
      - .actual_access:  write_only
        .address_space:  global
        .offset:         72
        .size:           8
        .value_kind:     global_buffer
      - .actual_access:  write_only
        .address_space:  global
        .offset:         80
        .size:           8
        .value_kind:     global_buffer
    .group_segment_fixed_size: 90112
    .kernarg_segment_align: 8
    .kernarg_segment_size: 88
    .language:       OpenCL C
    .language_version:
      - 2
      - 0
    .max_flat_workgroup_size: 768
    .name:           _Z7k_gemm1PKfS0_PKDv4_jPKiPiS6_P15HIP_vector_typeIiLj2EEPDF16_S0_S6_S9_
    .private_segment_fixed_size: 0
    .sgpr_count:     48
    .sgpr_spill_count: 0
    .symbol:         _Z7k_gemm1PKfS0_PKDv4_jPKiPiS6_P15HIP_vector_typeIiLj2EEPDF16_S0_S6_S9_.kd
    .uniform_work_group_size: 1
    .uses_dynamic_stack: false
    .vgpr_count:     168
    .vgpr_spill_count: 0
    .wavefront_size: 64
  - .agpr_count:     0
    .args:
      - .actual_access:  read_only
        .address_space:  global
        .offset:         0
        .size:           8
        .value_kind:     global_buffer
      - .actual_access:  read_only
        .address_space:  global
        .offset:         8
        .size:           8
        .value_kind:     global_buffer
      - .actual_access:  read_only
        .address_space:  global
        .offset:         16
        .size:           8
        .value_kind:     global_buffer
      - .actual_access:  read_only
        .address_space:  global
        .offset:         24
        .size:           8
        .value_kind:     global_buffer
      - .actual_access:  read_only
        .address_space:  global
        .offset:         32
        .size:           8
        .value_kind:     global_buffer
      - .actual_access:  read_only
        .address_space:  global
        .offset:         40
        .size:           8
        .value_kind:     global_buffer
      - .actual_access:  write_only
        .address_space:  global
        .offset:         48
        .size:           8
        .value_kind:     global_buffer
    .group_segment_fixed_size: 12576
    .kernarg_segment_align: 8
    .kernarg_segment_size: 56
    .language:       OpenCL C
    .language_version:
      - 2
      - 0
    .max_flat_workgroup_size: 256
    .name:           _Z8k_agg1g2PKDv4_jPKiS3_PK15HIP_vector_typeIiLj2EEPKfS1_PDF16_
    .private_segment_fixed_size: 0
    .sgpr_count:     52
    .sgpr_spill_count: 0
    .symbol:         _Z8k_agg1g2PKDv4_jPKiS3_PK15HIP_vector_typeIiLj2EEPKfS1_PDF16_.kd
    .uniform_work_group_size: 1
    .uses_dynamic_stack: false
    .vgpr_count:     126
    .vgpr_spill_count: 0
    .wavefront_size: 64
  - .agpr_count:     0
    .args:
      - .actual_access:  read_only
        .address_space:  global
        .offset:         0
        .size:           8
        .value_kind:     global_buffer
      - .actual_access:  read_only
        .address_space:  global
        .offset:         8
        .size:           8
        .value_kind:     global_buffer
      - .actual_access:  read_only
        .address_space:  global
        .offset:         16
        .size:           8
        .value_kind:     global_buffer
      - .actual_access:  read_only
        .address_space:  global
        .offset:         24
        .size:           8
        .value_kind:     global_buffer
      - .actual_access:  read_only
        .address_space:  global
        .offset:         32
        .size:           8
        .value_kind:     global_buffer
      - .actual_access:  write_only
        .address_space:  global
        .offset:         40
        .size:           8
        .value_kind:     global_buffer
      - .actual_access:  write_only
        .address_space:  global
        .offset:         48
        .size:           8
        .value_kind:     global_buffer
      - .actual_access:  write_only
        .address_space:  global
        .offset:         56
        .size:           8
        .value_kind:     global_buffer
    .group_segment_fixed_size: 0
    .kernarg_segment_align: 8
    .kernarg_segment_size: 64
    .language:       OpenCL C
    .language_version:
      - 2
      - 0
    .max_flat_workgroup_size: 256
    .name:           _Z6k_agg2PKDv4_jPKiS3_PK15HIP_vector_typeIiLj2EEPKfPfSA_PS_
    .private_segment_fixed_size: 0
    .sgpr_count:     18
    .sgpr_spill_count: 0
    .symbol:         _Z6k_agg2PKDv4_jPKiS3_PK15HIP_vector_typeIiLj2EEPKfPfSA_PS_.kd
    .uniform_work_group_size: 1
    .uses_dynamic_stack: false
    .vgpr_count:     74
    .vgpr_spill_count: 0
    .wavefront_size: 64
  - .agpr_count:     0
    .args:
      - .actual_access:  read_only
        .address_space:  global
        .offset:         0
        .size:           8
        .value_kind:     global_buffer
      - .actual_access:  read_only
        .address_space:  global
        .offset:         8
        .size:           8
        .value_kind:     global_buffer
      - .actual_access:  read_only
        .address_space:  global
        .offset:         16
        .size:           8
        .value_kind:     global_buffer
      - .actual_access:  read_only
        .address_space:  global
        .offset:         24
        .size:           8
        .value_kind:     global_buffer
      - .actual_access:  read_only
        .address_space:  global
        .offset:         32
        .size:           8
        .value_kind:     global_buffer
      - .actual_access:  read_only
        .address_space:  global
        .offset:         40
        .size:           8
        .value_kind:     global_buffer
      - .actual_access:  read_only
        .address_space:  global
        .offset:         48
        .size:           8
        .value_kind:     global_buffer
      - .actual_access:  write_only
        .address_space:  global
        .offset:         56
        .size:           8
        .value_kind:     global_buffer
      - .actual_access:  write_only
        .address_space:  global
        .offset:         64
        .size:           8
        .value_kind:     global_buffer
    .group_segment_fixed_size: 6144
    .kernarg_segment_align: 8
    .kernarg_segment_size: 72
    .language:       OpenCL C
    .language_version:
      - 2
      - 0
    .max_flat_workgroup_size: 256
    .name:           _Z9k_readoutPKDv4_jPKfPKiPK15HIP_vector_typeIiLj2EES3_S3_S3_PfSA_
    .private_segment_fixed_size: 0
    .sgpr_count:     36
    .sgpr_spill_count: 0
    .symbol:         _Z9k_readoutPKDv4_jPKfPKiPK15HIP_vector_typeIiLj2EES3_S3_S3_PfSA_.kd
    .uniform_work_group_size: 1
    .uses_dynamic_stack: false
    .vgpr_count:     94
    .vgpr_spill_count: 0
    .wavefront_size: 64
